# all-in + dnhoist: down-proj epilogue bias loads issued in the last K iteration, epilogue-head wait vmcnt(6) instead of a full drain
# baseline (speedup 1.0000x reference)
.LBB0_800:
	s_cmp_eq_u32 s91, 4
	s_cbranch_scc0 .Ldh_0
	s_cmp_lg_u64 s[40:41], 0
	s_cbranch_scc0 .Ldh_0
	s_lshl_b32 s100, s56, 12
	s_add_u32 s100, s16, s100
	s_addc_u32 s101, s17, 0
	v_lshl_or_b32 v236, s57, 8, v198
	v_mov_b32_e32 v237, 0
	v_lshl_add_u64 v[236:237], v[236:237], 2, s[100:101]
	global_load_dwordx4 v[224:227], v[236:237], off
	global_load_dwordx4 v[228:231], v[236:237], off offset:16
	global_load_dwordx4 v[232:235], v[236:237], off offset:512
	s_nop 0
	global_load_dwordx4 v[236:239], v[236:237], off offset:528

.LBB0_815:
	v_lshl_or_b32 v18, s57, 8, v198
	s_ashr_i32 s57, s56, 31
	s_lshl_b64 s[4:5], s[56:57], 12
	s_add_u32 s4, s16, s4
	s_addc_u32 s5, s17, s5
	v_ashrrev_i32_e32 v19, 31, v18
	v_cndmask_b32_e64 v3, 0, 1, s[40:41]
	v_lshl_add_u64 v[20:21], v[18:19], 2, s[4:5]
	v_mov_b32_e32 v2, 0
	v_cmp_ne_u32_e64 s[4:5], 1, v3
	s_andn2_b64 vcc, exec, s[40:41]
	v_mov_b32_e32 v6, 0
	v_mov_b32_e32 v7, 0
	v_mov_b32_e32 v8, 0
	v_mov_b32_e32 v9, 0
	s_cbranch_vccnz .LBB0_817
	v_mov_b32_e32 v6, v224
	v_mov_b32_e32 v7, v225
	v_mov_b32_e32 v8, v226
	v_mov_b32_e32 v9, v227
.LBB0_817:
	s_and_b64 vcc, exec, s[4:5]
	v_mov_b32_e32 v3, 0
	v_mov_b32_e32 v4, 0
	v_mov_b32_e32 v5, 0
	s_cbranch_vccnz .LBB0_819
	v_mov_b32_e32 v2, v228
	v_mov_b32_e32 v3, v229
	v_mov_b32_e32 v4, v230
	v_mov_b32_e32 v5, v231
.LBB0_819:
	v_mov_b32_e32 v10, 0
	s_and_b64 vcc, exec, s[4:5]
	v_mov_b32_e32 v14, 0
	v_mov_b32_e32 v15, 0
	v_mov_b32_e32 v16, 0
	v_mov_b32_e32 v17, 0
	s_cbranch_vccnz .LBB0_821
	v_mov_b32_e32 v14, v232
	v_mov_b32_e32 v15, v233
	v_mov_b32_e32 v16, v234
	v_mov_b32_e32 v17, v235
.LBB0_821:
	s_and_b64 vcc, exec, s[4:5]
	v_mov_b32_e32 v11, 0
	v_mov_b32_e32 v12, 0
	v_mov_b32_e32 v13, 0
	s_cbranch_vccnz .LBB0_823
	v_mov_b32_e32 v10, v236
	v_mov_b32_e32 v11, v237
	v_mov_b32_e32 v12, v238
	v_mov_b32_e32 v13, v239
.LBB0_823:
	v_lshl_add_u32 v20, s87, 8, v197
	v_ashrrev_i32_e32 v21, 31, v20
	v_lshlrev_b64 v[26:27], 11, v[20:21]
	v_lshl_add_u64 v[26:27], s[38:39], 0, v[26:27]
	v_lshlrev_b64 v[30:31], 1, v[18:19]
	v_lshl_add_u64 v[18:19], v[26:27], 0, v[30:31]
	s_waitcnt vmcnt(6)
	v_pk_fma_f32 v[26:27], v[190:191], s[44:45], v[6:7] op_sel_hi:[1,0,1]
	v_pk_fma_f32 v[28:29], v[192:193], s[44:45], v[8:9] op_sel_hi:[1,0,1]
	v_cvt_pk_bf16_f32 v26, v26, v27
	v_pk_fma_f32 v[32:33], v[188:189], s[44:45], v[4:5] op_sel_hi:[1,0,1]
	v_cvt_pk_bf16_f32 v27, v28, v29
	v_pk_fma_f32 v[34:35], v[186:187], s[44:45], v[2:3] op_sel_hi:[1,0,1]
	v_pk_fma_f32 v[36:37], v[170:171], s[44:45], v[2:3] op_sel_hi:[1,0,1]
	v_cvt_pk_bf16_f32 v28, v34, v35
	v_cvt_pk_bf16_f32 v29, v32, v33
	ds_write_b128 v240, v[26:29]
	s_waitcnt lgkmcnt(0)
	s_barrier
	ds_read_b128 v[246:249], v241
	v_lshl_add_u64 v[244:245], v[18:19], 0, v[242:243]
	v_pk_fma_f32 v[32:33], v[176:177], s[44:45], v[12:13] op_sel_hi:[1,0,1]
	v_pk_fma_f32 v[34:35], v[174:175], s[44:45], v[10:11] op_sel_hi:[1,0,1]
	v_pk_fma_f32 v[26:27], v[182:183], s[44:45], v[14:15] op_sel_hi:[1,0,1]
	v_pk_fma_f32 v[28:29], v[184:185], s[44:45], v[16:17] op_sel_hi:[1,0,1]
	v_cvt_pk_bf16_f32 v26, v26, v27
	s_mov_b64 s[4:5], 0x40000
	v_cvt_pk_bf16_f32 v27, v28, v29
	v_cvt_pk_bf16_f32 v28, v34, v35
	v_cvt_pk_bf16_f32 v29, v32, v33
	ds_write_b128 v240, v[26:29] offset:8192
	s_waitcnt lgkmcnt(1)
	global_store_dwordx4 v[244:245], v[246:249], off
	s_waitcnt lgkmcnt(0)
	s_barrier
	ds_read_b128 v[246:249], v241 offset:8192
	v_lshl_add_u64 v[244:245], v[18:19], 0, v[242:243]
	v_pk_fma_f32 v[34:35], v[172:173], s[44:45], v[4:5] op_sel_hi:[1,0,1]
	s_nop 0
	v_or_b32_e32 v26, 16, v20
	v_ashrrev_i32_e32 v27, 31, v26
	v_lshlrev_b64 v[26:27], 11, v[26:27]
	v_lshl_add_u64 v[26:27], s[38:39], 0, v[26:27]
	v_lshl_add_u64 v[32:33], v[26:27], 0, v[30:31]
	v_pk_fma_f32 v[26:27], v[178:179], s[44:45], v[6:7] op_sel_hi:[1,0,1]
	v_pk_fma_f32 v[28:29], v[180:181], s[44:45], v[8:9] op_sel_hi:[1,0,1]
	v_cvt_pk_bf16_f32 v26, v26, v27
	s_nop 0
	v_cvt_pk_bf16_f32 v27, v28, v29
	v_cvt_pk_bf16_f32 v28, v36, v37
	v_cvt_pk_bf16_f32 v29, v34, v35
	ds_write_b128 v240, v[26:29]
	s_waitcnt lgkmcnt(1)
	global_store_dwordx4 v[244:245], v[246:249], off offset:256
	s_waitcnt lgkmcnt(0)
	s_barrier
	ds_read_b128 v[246:249], v241
	v_lshl_add_u64 v[244:245], v[32:33], 0, v[242:243]
	v_pk_fma_f32 v[34:35], v[160:161], s[44:45], v[12:13] op_sel_hi:[1,0,1]
	v_pk_fma_f32 v[36:37], v[158:159], s[44:45], v[10:11] op_sel_hi:[1,0,1]
	v_pk_fma_f32 v[26:27], v[166:167], s[44:45], v[14:15] op_sel_hi:[1,0,1]
	v_pk_fma_f32 v[28:29], v[168:169], s[44:45], v[16:17] op_sel_hi:[1,0,1]
	v_cvt_pk_bf16_f32 v26, v26, v27
	s_nop 0
	v_cvt_pk_bf16_f32 v27, v28, v29
	v_cvt_pk_bf16_f32 v28, v36, v37
	v_cvt_pk_bf16_f32 v29, v34, v35
	ds_write_b128 v240, v[26:29] offset:8192
	s_waitcnt lgkmcnt(1)
	global_store_dwordx4 v[244:245], v[246:249], off
	s_waitcnt lgkmcnt(0)
	s_barrier
	ds_read_b128 v[246:249], v241 offset:8192
	v_lshl_add_u64 v[244:245], v[32:33], 0, v[242:243]
	v_pk_fma_f32 v[34:35], v[156:157], s[44:45], v[4:5] op_sel_hi:[1,0,1]
	v_pk_fma_f32 v[36:37], v[154:155], s[44:45], v[2:3] op_sel_hi:[1,0,1]
	v_or_b32_e32 v26, 32, v20
	v_ashrrev_i32_e32 v27, 31, v26
	v_lshlrev_b64 v[26:27], 11, v[26:27]
	v_lshl_add_u64 v[26:27], s[38:39], 0, v[26:27]
	v_lshl_add_u64 v[32:33], v[26:27], 0, v[30:31]
	v_pk_fma_f32 v[28:29], v[164:165], s[44:45], v[8:9] op_sel_hi:[1,0,1]
	v_pk_fma_f32 v[26:27], v[162:163], s[44:45], v[6:7] op_sel_hi:[1,0,1]
	v_or_b32_e32 v20, 48, v20
	v_cvt_pk_bf16_f32 v26, v26, v27
	v_cvt_pk_bf16_f32 v27, v28, v29
	v_cvt_pk_bf16_f32 v28, v36, v37
	v_cvt_pk_bf16_f32 v29, v34, v35
	ds_write_b128 v240, v[26:29]
	s_waitcnt lgkmcnt(1)
	global_store_dwordx4 v[244:245], v[246:249], off offset:256
	s_waitcnt lgkmcnt(0)
	s_barrier
	ds_read_b128 v[246:249], v241
	v_lshl_add_u64 v[244:245], v[32:33], 0, v[242:243]
	v_ashrrev_i32_e32 v21, 31, v20
	v_pk_fma_f32 v[34:35], v[144:145], s[44:45], v[12:13] op_sel_hi:[1,0,1]
	v_pk_fma_f32 v[28:29], v[152:153], s[44:45], v[16:17] op_sel_hi:[1,0,1]
	v_pk_fma_f32 v[26:27], v[150:151], s[44:45], v[14:15] op_sel_hi:[1,0,1]
	v_pk_fma_f32 v[36:37], v[142:143], s[44:45], v[10:11] op_sel_hi:[1,0,1]
	v_cvt_pk_bf16_f32 v26, v26, v27
	v_cvt_pk_bf16_f32 v27, v28, v29
	v_lshlrev_b64 v[20:21], 11, v[20:21]
	v_cvt_pk_bf16_f32 v28, v36, v37
	v_cvt_pk_bf16_f32 v29, v34, v35
	ds_write_b128 v240, v[26:29] offset:8192
	s_waitcnt lgkmcnt(1)
	global_store_dwordx4 v[244:245], v[246:249], off
	s_waitcnt lgkmcnt(0)
	s_barrier
	ds_read_b128 v[246:249], v241 offset:8192
	v_lshl_add_u64 v[244:245], v[32:33], 0, v[242:243]
	v_lshl_add_u64 v[20:21], s[38:39], 0, v[20:21]
	v_lshl_add_u64 v[20:21], v[20:21], 0, v[30:31]
	v_pk_fma_f32 v[28:29], v[148:149], s[44:45], v[8:9] op_sel_hi:[1,0,1]
	v_pk_fma_f32 v[26:27], v[146:147], s[44:45], v[6:7] op_sel_hi:[1,0,1]
	v_pk_fma_f32 v[30:31], v[140:141], s[44:45], v[4:5] op_sel_hi:[1,0,1]
	v_pk_fma_f32 v[32:33], v[138:139], s[44:45], v[2:3] op_sel_hi:[1,0,1]
	v_cvt_pk_bf16_f32 v26, v26, v27
	v_cvt_pk_bf16_f32 v27, v28, v29
	s_nop 0
	v_cvt_pk_bf16_f32 v28, v32, v33
	v_cvt_pk_bf16_f32 v29, v30, v31
	ds_write_b128 v240, v[26:29]
	s_waitcnt lgkmcnt(1)
	global_store_dwordx4 v[244:245], v[246:249], off offset:256
	s_waitcnt lgkmcnt(0)
	s_barrier
	ds_read_b128 v[246:249], v241
	v_lshl_add_u64 v[244:245], v[20:21], 0, v[242:243]
	v_pk_fma_f32 v[30:31], v[132:133], s[44:45], v[12:13] op_sel_hi:[1,0,1]
	v_pk_fma_f32 v[32:33], v[130:131], s[44:45], v[10:11] op_sel_hi:[1,0,1]
	v_pk_fma_f32 v[28:29], v[136:137], s[44:45], v[16:17] op_sel_hi:[1,0,1]
	v_pk_fma_f32 v[26:27], v[134:135], s[44:45], v[14:15] op_sel_hi:[1,0,1]
	s_nop 0
	v_cvt_pk_bf16_f32 v26, v26, v27
	v_cvt_pk_bf16_f32 v27, v28, v29
	v_cvt_pk_bf16_f32 v28, v32, v33
	v_cvt_pk_bf16_f32 v29, v30, v31
	ds_write_b128 v240, v[26:29] offset:8192
	s_waitcnt lgkmcnt(1)
	global_store_dwordx4 v[244:245], v[246:249], off
	s_waitcnt lgkmcnt(0)
	s_barrier
	ds_read_b128 v[246:249], v241 offset:8192
	v_lshl_add_u64 v[244:245], v[20:21], 0, v[242:243]
	v_pk_fma_f32 v[30:31], v[124:125], s[44:45], v[4:5] op_sel_hi:[1,0,1]
	v_pk_fma_f32 v[32:33], v[122:123], s[44:45], v[2:3] op_sel_hi:[1,0,1]
	v_pk_fma_f32 v[28:29], v[128:129], s[44:45], v[8:9] op_sel_hi:[1,0,1]
	v_pk_fma_f32 v[26:27], v[126:127], s[44:45], v[6:7] op_sel_hi:[1,0,1]
	v_lshl_add_u64 v[20:21], v[18:19], 0, s[4:5]
	v_cvt_pk_bf16_f32 v26, v26, v27
	v_cvt_pk_bf16_f32 v27, v28, v29
	v_cvt_pk_bf16_f32 v28, v32, v33
	v_cvt_pk_bf16_f32 v29, v30, v31
	v_add_co_u32_e32 v30, vcc, s83, v18
	v_pk_fma_f32 v[32:33], v[110:111], s[44:45], v[10:11] op_sel_hi:[1,0,1]
	s_nop 0
	v_addc_co_u32_e32 v31, vcc, 0, v19, vcc
	ds_write_b128 v240, v[26:29]
	s_waitcnt lgkmcnt(1)
	global_store_dwordx4 v[244:245], v[246:249], off offset:256
	s_waitcnt lgkmcnt(0)
	s_barrier
	ds_read_b128 v[246:249], v241
	v_lshl_add_u64 v[244:245], v[30:31], 0, v[242:243]
	v_pk_fma_f32 v[30:31], v[112:113], s[44:45], v[12:13] op_sel_hi:[1,0,1]
	s_mov_b64 s[4:5], -1
	v_pk_fma_f32 v[28:29], v[120:121], s[44:45], v[16:17] op_sel_hi:[1,0,1]
	v_pk_fma_f32 v[26:27], v[118:119], s[44:45], v[14:15] op_sel_hi:[1,0,1]
	s_nop 0
	v_cvt_pk_bf16_f32 v26, v26, v27
	v_cvt_pk_bf16_f32 v27, v28, v29
	v_cvt_pk_bf16_f32 v28, v32, v33
	v_cvt_pk_bf16_f32 v29, v30, v31
	ds_write_b128 v240, v[26:29] offset:8192
	s_waitcnt lgkmcnt(1)
	global_store_dwordx4 v[244:245], v[246:249], off
	s_waitcnt lgkmcnt(0)
	s_barrier
	ds_read_b128 v[246:249], v241 offset:8192
	v_lshl_add_u64 v[244:245], v[20:21], 0, v[242:243]
	v_pk_fma_f32 v[30:31], v[108:109], s[44:45], v[4:5] op_sel_hi:[1,0,1]
	v_pk_fma_f32 v[32:33], v[106:107], s[44:45], v[2:3] op_sel_hi:[1,0,1]
	v_pk_fma_f32 v[28:29], v[116:117], s[44:45], v[8:9] op_sel_hi:[1,0,1]
	v_pk_fma_f32 v[26:27], v[114:115], s[44:45], v[6:7] op_sel_hi:[1,0,1]
	v_lshl_add_u64 v[20:21], v[18:19], 0, s[46:47]
	v_cvt_pk_bf16_f32 v26, v26, v27
	v_cvt_pk_bf16_f32 v27, v28, v29
	v_cvt_pk_bf16_f32 v28, v32, v33
	v_cvt_pk_bf16_f32 v29, v30, v31
	v_add_co_u32_e32 v30, vcc, s84, v18
	v_pk_fma_f32 v[32:33], v[94:95], s[44:45], v[10:11] op_sel_hi:[1,0,1]
	s_nop 0
	v_addc_co_u32_e32 v31, vcc, 0, v19, vcc
	ds_write_b128 v240, v[26:29]
	s_waitcnt lgkmcnt(1)
	global_store_dwordx4 v[244:245], v[246:249], off offset:256
	s_waitcnt lgkmcnt(0)
	s_barrier
	ds_read_b128 v[246:249], v241
	v_lshl_add_u64 v[244:245], v[30:31], 0, v[242:243]
	v_pk_fma_f32 v[30:31], v[96:97], s[44:45], v[12:13] op_sel_hi:[1,0,1]
	s_nop 0
	v_pk_fma_f32 v[28:29], v[104:105], s[44:45], v[16:17] op_sel_hi:[1,0,1]
	v_pk_fma_f32 v[26:27], v[102:103], s[44:45], v[14:15] op_sel_hi:[1,0,1]
	s_nop 0
	v_cvt_pk_bf16_f32 v26, v26, v27
	v_cvt_pk_bf16_f32 v27, v28, v29
	v_cvt_pk_bf16_f32 v28, v32, v33
	v_cvt_pk_bf16_f32 v29, v30, v31
	ds_write_b128 v240, v[26:29] offset:8192
	s_waitcnt lgkmcnt(1)
	global_store_dwordx4 v[244:245], v[246:249], off
	s_waitcnt lgkmcnt(0)
	s_barrier
	ds_read_b128 v[246:249], v241 offset:8192
	v_lshl_add_u64 v[244:245], v[20:21], 0, v[242:243]
	v_pk_fma_f32 v[30:31], v[92:93], s[44:45], v[4:5] op_sel_hi:[1,0,1]
	v_pk_fma_f32 v[32:33], v[90:91], s[44:45], v[2:3] op_sel_hi:[1,0,1]
	v_pk_fma_f32 v[28:29], v[100:101], s[44:45], v[8:9] op_sel_hi:[1,0,1]
	v_pk_fma_f32 v[26:27], v[98:99], s[44:45], v[6:7] op_sel_hi:[1,0,1]
	v_lshl_add_u64 v[20:21], v[18:19], 0, s[48:49]
	v_cvt_pk_bf16_f32 v26, v26, v27
	v_cvt_pk_bf16_f32 v27, v28, v29
	v_cvt_pk_bf16_f32 v28, v32, v33
	v_cvt_pk_bf16_f32 v29, v30, v31
	v_add_co_u32_e32 v30, vcc, s85, v18
	v_pk_fma_f32 v[6:7], v[82:83], s[44:45], v[6:7] op_sel_hi:[1,0,1]
	s_nop 0
	v_addc_co_u32_e32 v31, vcc, 0, v19, vcc
	ds_write_b128 v240, v[26:29]
	s_waitcnt lgkmcnt(1)
	global_store_dwordx4 v[244:245], v[246:249], off offset:256
	s_waitcnt lgkmcnt(0)
	s_barrier
	ds_read_b128 v[246:249], v241
	v_lshl_add_u64 v[244:245], v[30:31], 0, v[242:243]
	v_pk_fma_f32 v[30:31], v[80:81], s[44:45], v[12:13] op_sel_hi:[1,0,1]
	v_pk_fma_f32 v[32:33], v[78:79], s[44:45], v[10:11] op_sel_hi:[1,0,1]
	v_pk_fma_f32 v[26:27], v[86:87], s[44:45], v[14:15] op_sel_hi:[1,0,1]
	v_pk_fma_f32 v[28:29], v[88:89], s[44:45], v[16:17] op_sel_hi:[1,0,1]
	v_cvt_pk_bf16_f32 v26, v26, v27
	v_pk_fma_f32 v[8:9], v[84:85], s[44:45], v[8:9] op_sel_hi:[1,0,1]
	v_cvt_pk_bf16_f32 v27, v28, v29
	v_cvt_pk_bf16_f32 v28, v32, v33
	v_cvt_pk_bf16_f32 v29, v30, v31
	ds_write_b128 v240, v[26:29] offset:8192
	s_waitcnt lgkmcnt(1)
	global_store_dwordx4 v[244:245], v[246:249], off
	s_waitcnt lgkmcnt(0)
	s_barrier
	ds_read_b128 v[246:249], v241 offset:8192
	v_lshl_add_u64 v[244:245], v[20:21], 0, v[242:243]
	v_lshl_add_u64 v[20:21], v[18:19], 0, s[50:51]
	s_nop 0
	v_pk_fma_f32 v[26:27], v[76:77], s[44:45], v[4:5] op_sel_hi:[1,0,1]
	v_pk_fma_f32 v[4:5], v[74:75], s[44:45], v[2:3] op_sel_hi:[1,0,1]
	v_cvt_pk_bf16_f32 v2, v6, v7
	v_add_co_u32_e32 v6, vcc, s86, v18
	v_cvt_pk_bf16_f32 v3, v8, v9
	v_cvt_pk_bf16_f32 v4, v4, v5
	v_cvt_pk_bf16_f32 v5, v26, v27
	v_pk_fma_f32 v[8:9], v[66:67], s[44:45], v[10:11] op_sel_hi:[1,0,1]
	s_nop 0
	v_addc_co_u32_e32 v7, vcc, 0, v19, vcc
	ds_write_b128 v240, v[2:5]
	s_waitcnt lgkmcnt(1)
	global_store_dwordx4 v[244:245], v[246:249], off offset:256
	s_waitcnt lgkmcnt(0)
	s_barrier
	ds_read_b128 v[246:249], v241
	v_lshl_add_u64 v[244:245], v[6:7], 0, v[242:243]
	s_andn2_b64 vcc, exec, s[54:55]
	v_pk_fma_f32 v[6:7], v[68:69], s[44:45], v[12:13] op_sel_hi:[1,0,1]
	v_pk_fma_f32 v[4:5], v[72:73], s[44:45], v[16:17] op_sel_hi:[1,0,1]
	v_pk_fma_f32 v[2:3], v[70:71], s[44:45], v[14:15] op_sel_hi:[1,0,1]
	s_nop 0
	v_cvt_pk_bf16_f32 v2, v2, v3
	v_cvt_pk_bf16_f32 v3, v4, v5
	v_cvt_pk_bf16_f32 v4, v8, v9
	v_cvt_pk_bf16_f32 v5, v6, v7
	ds_write_b128 v240, v[2:5] offset:8192
	s_waitcnt lgkmcnt(1)
	global_store_dwordx4 v[244:245], v[246:249], off
	s_waitcnt lgkmcnt(0)
	s_barrier
	ds_read_b128 v[246:249], v241 offset:8192
	v_lshl_add_u64 v[244:245], v[20:21], 0, v[242:243]
	s_waitcnt lgkmcnt(0)
	s_barrier
	global_store_dwordx4 v[244:245], v[246:249], off offset:256
	s_cbranch_vccnz .LBB0_789
	s_andn2_b64 vcc, exec, s[28:29]
	s_cbranch_vccnz .LBB0_788
	s_barrier
	s_branch .LBB0_788

.LBB0_1876:
	s_cmp_eq_u32 s87, 4
	s_cbranch_scc0 .Ldh_1
	s_lshl_b32 s100, s48, 12
	s_add_u32 s100, s72, s100
	s_addc_u32 s101, s73, 0
	v_lshl_or_b32 v236, s49, 8, v196
	v_mov_b32_e32 v237, 0
	v_lshl_add_u64 v[236:237], v[236:237], 2, s[100:101]
	global_load_dwordx4 v[224:227], v[236:237], off
	global_load_dwordx4 v[228:231], v[236:237], off offset:16
	global_load_dwordx4 v[232:235], v[236:237], off offset:512
	s_nop 0
	global_load_dwordx4 v[236:239], v[236:237], off offset:528

.LBB0_1891:
	v_lshl_or_b32 v18, s49, 8, v196
	s_ashr_i32 s49, s48, 31
	s_lshl_b64 s[48:49], s[48:49], 12
	s_add_u32 s48, s72, s48
	s_addc_u32 s49, s73, s49
	v_ashrrev_i32_e32 v19, 31, v18
	v_lshl_add_u64 v[2:3], v[18:19], 2, s[48:49]
	v_mov_b32_e32 v14, v224
	v_mov_b32_e32 v15, v225
	v_mov_b32_e32 v16, v226
	v_mov_b32_e32 v17, v227
	v_mov_b32_e32 v10, v228
	v_mov_b32_e32 v11, v229
	v_mov_b32_e32 v12, v230
	v_mov_b32_e32 v13, v231
	v_mov_b32_e32 v6, v232
	v_mov_b32_e32 v7, v233
	v_mov_b32_e32 v8, v234
	v_mov_b32_e32 v9, v235
	s_nop 0
	v_mov_b32_e32 v2, v236
	v_mov_b32_e32 v3, v237
	v_mov_b32_e32 v4, v238
	v_mov_b32_e32 v5, v239
	v_lshl_add_u32 v24, s84, 8, v195
	v_ashrrev_i32_e32 v25, 31, v24
	v_or_b32_e32 v26, 16, v24
	v_or_b32_e32 v28, 32, v24
	v_or_b32_e32 v30, 48, v24
	v_lshlrev_b64 v[24:25], 11, v[24:25]
	v_ashrrev_i32_e32 v27, 31, v26
	v_ashrrev_i32_e32 v29, 31, v28
	v_lshlrev_b64 v[32:33], 1, v[18:19]
	v_ashrrev_i32_e32 v31, 31, v30
	v_lshl_add_u64 v[18:19], s[28:29], 0, v[24:25]
	v_lshlrev_b64 v[24:25], 11, v[26:27]
	v_lshlrev_b64 v[26:27], 11, v[28:29]
	v_lshlrev_b64 v[28:29], 11, v[30:31]
	v_lshl_add_u64 v[24:25], s[28:29], 0, v[24:25]
	v_lshl_add_u64 v[26:27], s[28:29], 0, v[26:27]
	v_lshl_add_u64 v[28:29], s[28:29], 0, v[28:29]
	v_lshl_add_u64 v[30:31], v[24:25], 0, v[32:33]
	v_lshl_add_u64 v[34:35], v[26:27], 0, v[32:33]
	v_lshl_add_u64 v[18:19], v[18:19], 0, v[32:33]
	v_lshl_add_u64 v[28:29], v[28:29], 0, v[32:33]
	s_waitcnt vmcnt(6)
	v_pk_fma_f32 v[26:27], v[192:193], s[30:31], v[16:17] op_sel_hi:[1,0,1]
	v_pk_fma_f32 v[24:25], v[190:191], s[30:31], v[14:15] op_sel_hi:[1,0,1]
	v_pk_fma_f32 v[32:33], v[188:189], s[30:31], v[12:13] op_sel_hi:[1,0,1]
	v_pk_fma_f32 v[36:37], v[186:187], s[30:31], v[10:11] op_sel_hi:[1,0,1]
	v_cvt_pk_bf16_f32 v24, v24, v25
	v_cvt_pk_bf16_f32 v25, v26, v27
	v_pk_fma_f32 v[38:39], v[172:173], s[30:31], v[8:9] op_sel_hi:[1,0,1]
	v_cvt_pk_bf16_f32 v26, v36, v37
	v_cvt_pk_bf16_f32 v27, v32, v33
	v_pk_fma_f32 v[40:41], v[170:171], s[30:31], v[6:7] op_sel_hi:[1,0,1]
	v_pk_fma_f32 v[42:43], v[164:165], s[30:31], v[4:5] op_sel_hi:[1,0,1]
	v_pk_fma_f32 v[44:45], v[162:163], s[30:31], v[2:3] op_sel_hi:[1,0,1]
	ds_write_b128 v240, v[24:27]
	s_waitcnt lgkmcnt(0)
	s_barrier
	ds_read_b128 v[246:249], v241
	v_lshl_add_u64 v[244:245], v[18:19], 0, v[242:243]
	v_pk_fma_f32 v[46:47], v[184:185], s[30:31], v[16:17] op_sel_hi:[1,0,1]
	v_pk_fma_f32 v[48:49], v[182:183], s[30:31], v[14:15] op_sel_hi:[1,0,1]
	v_cvt_pk_bf16_f32 v24, v40, v41
	v_cvt_pk_bf16_f32 v25, v38, v39
	v_cvt_pk_bf16_f32 v26, v44, v45
	v_cvt_pk_bf16_f32 v27, v42, v43
	v_pk_fma_f32 v[50:51], v[180:181], s[30:31], v[12:13] op_sel_hi:[1,0,1]
	v_pk_fma_f32 v[52:53], v[178:179], s[30:31], v[10:11] op_sel_hi:[1,0,1]
	ds_write_b128 v240, v[24:27] offset:8192
	s_waitcnt lgkmcnt(1)
	global_store_dwordx4 v[244:245], v[246:249], off
	s_waitcnt lgkmcnt(0)
	s_barrier
	ds_read_b128 v[246:249], v241 offset:8192
	v_lshl_add_u64 v[244:245], v[18:19], 0, v[242:243]
	v_pk_fma_f32 v[54:55], v[156:157], s[30:31], v[8:9] op_sel_hi:[1,0,1]
	v_pk_fma_f32 v[56:57], v[154:155], s[30:31], v[6:7] op_sel_hi:[1,0,1]
	v_cvt_pk_bf16_f32 v24, v48, v49
	v_cvt_pk_bf16_f32 v25, v46, v47
	v_cvt_pk_bf16_f32 v26, v52, v53
	v_cvt_pk_bf16_f32 v27, v50, v51
	v_pk_fma_f32 v[58:59], v[148:149], s[30:31], v[4:5] op_sel_hi:[1,0,1]
	v_pk_fma_f32 v[60:61], v[146:147], s[30:31], v[2:3] op_sel_hi:[1,0,1]
	ds_write_b128 v240, v[24:27]
	s_waitcnt lgkmcnt(1)
	global_store_dwordx4 v[244:245], v[246:249], off offset:256
	s_waitcnt lgkmcnt(0)
	s_barrier
	ds_read_b128 v[246:249], v241
	v_lshl_add_u64 v[244:245], v[30:31], 0, v[242:243]
	v_pk_fma_f32 v[62:63], v[176:177], s[30:31], v[16:17] op_sel_hi:[1,0,1]
	v_pk_fma_f32 v[64:65], v[174:175], s[30:31], v[14:15] op_sel_hi:[1,0,1]
	v_cvt_pk_bf16_f32 v24, v56, v57
	v_cvt_pk_bf16_f32 v25, v54, v55
	v_cvt_pk_bf16_f32 v26, v60, v61
	v_cvt_pk_bf16_f32 v27, v58, v59
	v_pk_fma_f32 v[146:147], v[168:169], s[30:31], v[12:13] op_sel_hi:[1,0,1]
	v_pk_fma_f32 v[148:149], v[166:167], s[30:31], v[10:11] op_sel_hi:[1,0,1]
	ds_write_b128 v240, v[24:27] offset:8192
	s_waitcnt lgkmcnt(1)
	global_store_dwordx4 v[244:245], v[246:249], off
	s_waitcnt lgkmcnt(0)
	s_barrier
	ds_read_b128 v[246:249], v241 offset:8192
	v_lshl_add_u64 v[244:245], v[30:31], 0, v[242:243]
	v_pk_fma_f32 v[144:145], v[144:145], s[30:31], v[8:9] op_sel_hi:[1,0,1]
	v_pk_fma_f32 v[142:143], v[142:143], s[30:31], v[6:7] op_sel_hi:[1,0,1]
	v_cvt_pk_bf16_f32 v24, v64, v65
	v_cvt_pk_bf16_f32 v25, v62, v63
	v_cvt_pk_bf16_f32 v26, v148, v149
	v_cvt_pk_bf16_f32 v27, v146, v147
	v_pk_fma_f32 v[140:141], v[140:141], s[30:31], v[4:5] op_sel_hi:[1,0,1]
	v_pk_fma_f32 v[138:139], v[138:139], s[30:31], v[2:3] op_sel_hi:[1,0,1]
	ds_write_b128 v240, v[24:27]
	s_waitcnt lgkmcnt(1)
	global_store_dwordx4 v[244:245], v[246:249], off offset:256
	s_waitcnt lgkmcnt(0)
	s_barrier
	ds_read_b128 v[246:249], v241
	v_lshl_add_u64 v[244:245], v[34:35], 0, v[242:243]
	v_pk_fma_f32 v[154:155], v[160:161], s[30:31], v[16:17] op_sel_hi:[1,0,1]
	v_pk_fma_f32 v[156:157], v[158:159], s[30:31], v[14:15] op_sel_hi:[1,0,1]
	v_cvt_pk_bf16_f32 v24, v142, v143
	v_cvt_pk_bf16_f32 v25, v144, v145
	v_cvt_pk_bf16_f32 v26, v138, v139
	v_cvt_pk_bf16_f32 v27, v140, v141
	v_pk_fma_f32 v[152:153], v[152:153], s[30:31], v[12:13] op_sel_hi:[1,0,1]
	v_pk_fma_f32 v[150:151], v[150:151], s[30:31], v[10:11] op_sel_hi:[1,0,1]
	ds_write_b128 v240, v[24:27] offset:8192
	s_waitcnt lgkmcnt(1)
	global_store_dwordx4 v[244:245], v[246:249], off
	s_waitcnt lgkmcnt(0)
	s_barrier
	ds_read_b128 v[246:249], v241 offset:8192
	v_lshl_add_u64 v[244:245], v[34:35], 0, v[242:243]
	v_pk_fma_f32 v[30:31], v[132:133], s[30:31], v[4:5] op_sel_hi:[1,0,1]
	v_pk_fma_f32 v[32:33], v[130:131], s[30:31], v[2:3] op_sel_hi:[1,0,1]
	v_cvt_pk_bf16_f32 v24, v156, v157
	v_cvt_pk_bf16_f32 v25, v154, v155
	v_cvt_pk_bf16_f32 v26, v150, v151
	v_cvt_pk_bf16_f32 v27, v152, v153
	ds_write_b128 v240, v[24:27]
	s_waitcnt lgkmcnt(1)
	global_store_dwordx4 v[244:245], v[246:249], off offset:256
	s_waitcnt lgkmcnt(0)
	s_barrier
	ds_read_b128 v[246:249], v241
	v_lshl_add_u64 v[244:245], v[28:29], 0, v[242:243]
	s_nop 1
	v_pk_fma_f32 v[26:27], v[136:137], s[30:31], v[8:9] op_sel_hi:[1,0,1]
	v_pk_fma_f32 v[24:25], v[134:135], s[30:31], v[6:7] op_sel_hi:[1,0,1]
	s_nop 0
	v_cvt_pk_bf16_f32 v24, v24, v25
	v_cvt_pk_bf16_f32 v25, v26, v27
	v_cvt_pk_bf16_f32 v26, v32, v33
	v_cvt_pk_bf16_f32 v27, v30, v31
	ds_write_b128 v240, v[24:27] offset:8192
	s_waitcnt lgkmcnt(1)
	global_store_dwordx4 v[244:245], v[246:249], off
	s_waitcnt lgkmcnt(0)
	s_barrier
	ds_read_b128 v[246:249], v241 offset:8192
	v_lshl_add_u64 v[244:245], v[28:29], 0, v[242:243]
	v_pk_fma_f32 v[30:31], v[124:125], s[30:31], v[12:13] op_sel_hi:[1,0,1]
	v_pk_fma_f32 v[32:33], v[122:123], s[30:31], v[10:11] op_sel_hi:[1,0,1]
	v_pk_fma_f32 v[26:27], v[128:129], s[30:31], v[16:17] op_sel_hi:[1,0,1]
	v_pk_fma_f32 v[24:25], v[126:127], s[30:31], v[14:15] op_sel_hi:[1,0,1]
	v_lshl_add_u64 v[28:29], v[18:19], 0, s[38:39]
	v_cvt_pk_bf16_f32 v24, v24, v25
	v_cvt_pk_bf16_f32 v25, v26, v27
	v_cvt_pk_bf16_f32 v26, v32, v33
	v_cvt_pk_bf16_f32 v27, v30, v31
	v_add_co_u32_e32 v30, vcc, s80, v18
	v_pk_fma_f32 v[32:33], v[110:111], s[30:31], v[2:3] op_sel_hi:[1,0,1]
	s_nop 0
	v_addc_co_u32_e32 v31, vcc, 0, v19, vcc
	ds_write_b128 v240, v[24:27]
	s_waitcnt lgkmcnt(1)
	global_store_dwordx4 v[244:245], v[246:249], off offset:256
	s_waitcnt lgkmcnt(0)
	s_barrier
	ds_read_b128 v[246:249], v241
	v_lshl_add_u64 v[244:245], v[30:31], 0, v[242:243]
	v_pk_fma_f32 v[30:31], v[112:113], s[30:31], v[4:5] op_sel_hi:[1,0,1]
	s_nop 0
	v_pk_fma_f32 v[26:27], v[120:121], s[30:31], v[8:9] op_sel_hi:[1,0,1]
	v_pk_fma_f32 v[24:25], v[118:119], s[30:31], v[6:7] op_sel_hi:[1,0,1]
	s_nop 0
	v_cvt_pk_bf16_f32 v24, v24, v25
	v_cvt_pk_bf16_f32 v25, v26, v27
	v_cvt_pk_bf16_f32 v26, v32, v33
	v_cvt_pk_bf16_f32 v27, v30, v31
	ds_write_b128 v240, v[24:27] offset:8192
	s_waitcnt lgkmcnt(1)
	global_store_dwordx4 v[244:245], v[246:249], off
	s_waitcnt lgkmcnt(0)
	s_barrier
	ds_read_b128 v[246:249], v241 offset:8192
	v_lshl_add_u64 v[244:245], v[28:29], 0, v[242:243]
	v_pk_fma_f32 v[30:31], v[108:109], s[30:31], v[12:13] op_sel_hi:[1,0,1]
	v_pk_fma_f32 v[32:33], v[106:107], s[30:31], v[10:11] op_sel_hi:[1,0,1]
	v_pk_fma_f32 v[26:27], v[116:117], s[30:31], v[16:17] op_sel_hi:[1,0,1]
	v_pk_fma_f32 v[24:25], v[114:115], s[30:31], v[14:15] op_sel_hi:[1,0,1]
	v_lshl_add_u64 v[28:29], v[18:19], 0, s[40:41]
	v_cvt_pk_bf16_f32 v24, v24, v25
	v_cvt_pk_bf16_f32 v25, v26, v27
	v_cvt_pk_bf16_f32 v26, v32, v33
	v_cvt_pk_bf16_f32 v27, v30, v31
	v_add_co_u32_e32 v30, vcc, s81, v18
	v_pk_fma_f32 v[32:33], v[94:95], s[30:31], v[2:3] op_sel_hi:[1,0,1]
	s_nop 0
	v_addc_co_u32_e32 v31, vcc, 0, v19, vcc
	ds_write_b128 v240, v[24:27]
	s_waitcnt lgkmcnt(1)
	global_store_dwordx4 v[244:245], v[246:249], off offset:256
	s_waitcnt lgkmcnt(0)
	s_barrier
	ds_read_b128 v[246:249], v241
	v_lshl_add_u64 v[244:245], v[30:31], 0, v[242:243]
	v_pk_fma_f32 v[30:31], v[96:97], s[30:31], v[4:5] op_sel_hi:[1,0,1]
	s_nop 0
	v_pk_fma_f32 v[26:27], v[104:105], s[30:31], v[8:9] op_sel_hi:[1,0,1]
	v_pk_fma_f32 v[24:25], v[102:103], s[30:31], v[6:7] op_sel_hi:[1,0,1]
	s_nop 0
	v_cvt_pk_bf16_f32 v24, v24, v25
	v_cvt_pk_bf16_f32 v25, v26, v27
	v_cvt_pk_bf16_f32 v26, v32, v33
	v_cvt_pk_bf16_f32 v27, v30, v31
	ds_write_b128 v240, v[24:27] offset:8192
	s_waitcnt lgkmcnt(1)
	global_store_dwordx4 v[244:245], v[246:249], off
	s_waitcnt lgkmcnt(0)
	s_barrier
	ds_read_b128 v[246:249], v241 offset:8192
	v_lshl_add_u64 v[244:245], v[28:29], 0, v[242:243]
	v_pk_fma_f32 v[30:31], v[92:93], s[30:31], v[12:13] op_sel_hi:[1,0,1]
	v_pk_fma_f32 v[32:33], v[90:91], s[30:31], v[10:11] op_sel_hi:[1,0,1]
	v_pk_fma_f32 v[26:27], v[100:101], s[30:31], v[16:17] op_sel_hi:[1,0,1]
	v_pk_fma_f32 v[24:25], v[98:99], s[30:31], v[14:15] op_sel_hi:[1,0,1]
	v_lshl_add_u64 v[28:29], v[18:19], 0, s[42:43]
	v_cvt_pk_bf16_f32 v24, v24, v25
	v_cvt_pk_bf16_f32 v25, v26, v27
	v_cvt_pk_bf16_f32 v26, v32, v33
	v_cvt_pk_bf16_f32 v27, v30, v31
	v_add_co_u32_e32 v30, vcc, s82, v18
	v_pk_fma_f32 v[32:33], v[78:79], s[30:31], v[2:3] op_sel_hi:[1,0,1]
	s_nop 0
	v_addc_co_u32_e32 v31, vcc, 0, v19, vcc
	ds_write_b128 v240, v[24:27]
	s_waitcnt lgkmcnt(1)
	global_store_dwordx4 v[244:245], v[246:249], off offset:256
	s_waitcnt lgkmcnt(0)
	s_barrier
	ds_read_b128 v[246:249], v241
	v_lshl_add_u64 v[244:245], v[30:31], 0, v[242:243]
	v_pk_fma_f32 v[30:31], v[80:81], s[30:31], v[4:5] op_sel_hi:[1,0,1]
	v_pk_fma_f32 v[14:15], v[82:83], s[30:31], v[14:15] op_sel_hi:[1,0,1]
	v_pk_fma_f32 v[26:27], v[88:89], s[30:31], v[8:9] op_sel_hi:[1,0,1]
	v_pk_fma_f32 v[24:25], v[86:87], s[30:31], v[6:7] op_sel_hi:[1,0,1]
	v_pk_fma_f32 v[16:17], v[84:85], s[30:31], v[16:17] op_sel_hi:[1,0,1]
	v_cvt_pk_bf16_f32 v24, v24, v25
	v_cvt_pk_bf16_f32 v25, v26, v27
	v_cvt_pk_bf16_f32 v26, v32, v33
	v_cvt_pk_bf16_f32 v27, v30, v31
	ds_write_b128 v240, v[24:27] offset:8192
	s_waitcnt lgkmcnt(1)
	global_store_dwordx4 v[244:245], v[246:249], off
	s_waitcnt lgkmcnt(0)
	s_barrier
	ds_read_b128 v[246:249], v241 offset:8192
	v_lshl_add_u64 v[244:245], v[28:29], 0, v[242:243]
	v_pk_fma_f32 v[8:9], v[72:73], s[30:31], v[8:9] op_sel_hi:[1,0,1]
	v_pk_fma_f32 v[6:7], v[70:71], s[30:31], v[6:7] op_sel_hi:[1,0,1]
	v_pk_fma_f32 v[26:27], v[76:77], s[30:31], v[12:13] op_sel_hi:[1,0,1]
	v_pk_fma_f32 v[12:13], v[74:75], s[30:31], v[10:11] op_sel_hi:[1,0,1]
	v_cvt_pk_bf16_f32 v10, v14, v15
	v_add_co_u32_e32 v14, vcc, s83, v18
	v_cvt_pk_bf16_f32 v11, v16, v17
	v_lshl_add_u64 v[24:25], v[18:19], 0, s[44:45]
	s_nop 0
	v_addc_co_u32_e32 v15, vcc, 0, v19, vcc
	v_cvt_pk_bf16_f32 v12, v12, v13
	v_cvt_pk_bf16_f32 v13, v26, v27
	ds_write_b128 v240, v[10:13]
	s_waitcnt lgkmcnt(1)
	global_store_dwordx4 v[244:245], v[246:249], off offset:256
	s_waitcnt lgkmcnt(0)
	s_barrier
	ds_read_b128 v[246:249], v241
	v_lshl_add_u64 v[244:245], v[14:15], 0, v[242:243]
	s_andn2_b64 vcc, exec, s[46:47]
	s_mov_b64 s[46:47], -1
	v_pk_fma_f32 v[10:11], v[68:69], s[30:31], v[4:5] op_sel_hi:[1,0,1]
	v_pk_fma_f32 v[4:5], v[66:67], s[30:31], v[2:3] op_sel_hi:[1,0,1]
	v_cvt_pk_bf16_f32 v2, v6, v7
	v_cvt_pk_bf16_f32 v3, v8, v9
	s_nop 0
	v_cvt_pk_bf16_f32 v4, v4, v5
	v_cvt_pk_bf16_f32 v5, v10, v11
	ds_write_b128 v240, v[2:5] offset:8192
	s_waitcnt lgkmcnt(1)
	global_store_dwordx4 v[244:245], v[246:249], off
	s_waitcnt lgkmcnt(0)
	s_barrier
	ds_read_b128 v[246:249], v241 offset:8192
	v_lshl_add_u64 v[244:245], v[24:25], 0, v[242:243]
	s_waitcnt lgkmcnt(0)
	s_barrier
	global_store_dwordx4 v[244:245], v[246:249], off offset:256
	s_cbranch_vccnz .LBB0_1865
	s_andn2_b64 vcc, exec, s[20:21]
	s_cbranch_vccnz .LBB0_1864
	s_barrier
	s_branch .LBB0_1864
